# v44 + thin1->gate/up GEMM (odd sub-layers) grid barrier replaced by batch-group hand-off plus a chip-wide gate/up-phase-done guard for the converted weights
# baseline (speedup 1.0000x reference)
; __device__ __forceinline__ unsigned xb_ld(unsigned* p)              { return __hip_atomic_load(p, __ATOMIC_RELAXED, __HIP_MEMORY_SCOPE_AGENT); }
; __device__ __forceinline__ unsigned xb_add(unsigned* p, unsigned v) { return __hip_atomic_fetch_add(p, v, __ATOMIC_RELAXED, __HIP_MEMORY_SCOPE_AGENT); }
; #define XB_SPIN(cond, bar) do { unsigned _sp = 0; while (cond) { __builtin_amdgcn_s_sleep(1); \
;     if ((++_sp & 255u) == 0u) { if (xb_ld(&(bar)[XB_TMO])) break; if (_sp > XB_SPIN_CAP) { atomicAdd(&(bar)[XB_TMO], 1u); break; } } } } while (0)
; __device__ __forceinline__ void xcd_barrier(const XcdBarrier& b) {
;     asm volatile("s_waitcnt vmcnt(0)" ::: "memory");
;     __syncthreads();
;     if (threadIdx.x == 0) {
;         unsigned* bar = b.bar;
;         __builtin_amdgcn_s_waitcnt(0);
;         unsigned nloc = b.st[0], nx = b.st[1];
;         if (nloc == 0u) { xcd_barrier_complete(bar, b.x, nloc, nx); b.st[0] = nloc; b.st[1] = nx; }
;         const unsigned old = xb_add(&bar[XB_XSUB(b.x)], 1u);
;         const unsigned gen = old / nloc;
;         if (old + 1u == (gen + 1u) * nloc) {
;             __builtin_amdgcn_fence(__ATOMIC_RELEASE, "agent");
;             asm volatile("s_waitcnt vmcnt(0)" ::: "memory");
;             const unsigned og = xb_add(&bar[XB_TOP], 1u);
;             const unsigned tg = og / nx;
;             if (og + 1u == (tg + 1u) * nx) xb_add(&bar[XB_TOPGEN], 1u);
;             else XB_SPIN(xb_ld(&bar[XB_TOPGEN]) == tg, bar);
;             __builtin_amdgcn_fence(__ATOMIC_ACQUIRE, "agent");
;             xb_add(&bar[XB_XGEN(b.x)], 1u);
;             asm volatile("s_waitcnt vmcnt(0)" ::: "memory");
;         } else {
;             XB_SPIN(xb_ld(&bar[XB_XGEN(b.x)]) == gen, bar);
;             __builtin_amdgcn_fence(__ATOMIC_ACQUIRE, "agent");
;             asm volatile("s_waitcnt vmcnt(0)" ::: "memory");
;         }
;     }
;     __syncthreads();
; }
.LBB0_599:
	v_readlane_b32 s0, v253, 42
	v_readlane_b32 s4, v253, 32
	s_add_i32 s0, s0, 1
	v_readlane_b32 s7, v253, 35
	s_cmp_ge_i32 s0, s7
	v_readlane_b32 s5, v253, 33
	v_readlane_b32 s6, v253, 34
	s_cbranch_scc1 .LBB0_645
	v_readlane_b32 s34, v253, 36
	v_readlane_b32 s35, v253, 37
	s_mov_b32 s1, s76
	s_waitcnt vmcnt(0)
	s_waitcnt vmcnt(0) lgkmcnt(0)
	s_barrier
	s_mov_b64 s[40:41], exec
	v_readlane_b32 s2, v253, 53
	v_readlane_b32 s3, v253, 54
	s_and_b64 s[2:3], s[40:41], s[2:3]
	s_mov_b64 exec, s[2:3]
	s_cbranch_execz .LBB0_644
	v_readlane_b32 s10, v253, 36
	v_readlane_b32 s11, v253, 37
	s_nop 3
	s_add_u32 s12, s10, 0xb800
	s_addc_u32 s13, s11, 0
	s_and_b32 s15, s88, 7
	s_lshl_b32 s15, s15, 8
	v_mov_b32_e32 v2, s15
	v_mov_b32_e32 v5, 1
	global_atomic_add v2, v5, s[12:13]
	v_readlane_b32 s10, v253, 36
	v_readlane_b32 s11, v253, 37
	v_readlane_b32 s14, v253, 55
	s_nop 3
	s_add_u32 s12, s10, 0x5000
	s_addc_u32 s13, s11, 0
	s_and_b32 s15, s88, 7
	s_lshr_b32 s16, s88, 3
	s_lshl_b32 s15, s15, 3
	s_and_b32 s17, s16, 7
	s_add_i32 s17, s17, s15
	s_lshr_b32 s16, s16, 2
	s_add_i32 s16, s16, s15
	s_lshl_b32 s17, s17, 6
	s_lshl_b32 s16, s16, 6
	s_mov_b32 s16, s17
	s_add_i32 s14, s14, 1
	s_lshl_b32 s14, s14, 2
	v_mov_b32_e32 v2, s17
	v_mov_b32_e32 v5, 1
	v_mov_b32_e32 v4, s16
	global_atomic_add v2, v5, s[12:13]
	s_mov_b32 s18, 0

; __device__ __forceinline__ unsigned xb_ld(unsigned* p)              { return __hip_atomic_load(p, __ATOMIC_RELAXED, __HIP_MEMORY_SCOPE_AGENT); }
; __device__ __forceinline__ unsigned xb_add(unsigned* p, unsigned v) { return __hip_atomic_fetch_add(p, v, __ATOMIC_RELAXED, __HIP_MEMORY_SCOPE_AGENT); }
; #define XB_SPIN(cond, bar) do { unsigned _sp = 0; while (cond) { __builtin_amdgcn_s_sleep(1); \
;     if ((++_sp & 255u) == 0u) { if (xb_ld(&(bar)[XB_TMO])) break; if (_sp > XB_SPIN_CAP) { atomicAdd(&(bar)[XB_TMO], 1u); break; } } } } while (0)
; __device__ __forceinline__ void xcd_barrier(const XcdBarrier& b) {
;     asm volatile("s_waitcnt vmcnt(0)" ::: "memory");
;     __syncthreads();
;     if (threadIdx.x == 0) {
;         unsigned* bar = b.bar;
;         __builtin_amdgcn_s_waitcnt(0);
;         unsigned nloc = b.st[0], nx = b.st[1];
;         if (nloc == 0u) { xcd_barrier_complete(bar, b.x, nloc, nx); b.st[0] = nloc; b.st[1] = nx; }
;         const unsigned old = xb_add(&bar[XB_XSUB(b.x)], 1u);
;         const unsigned gen = old / nloc;
;         if (old + 1u == (gen + 1u) * nloc) {
;             __builtin_amdgcn_fence(__ATOMIC_RELEASE, "agent");
;             asm volatile("s_waitcnt vmcnt(0)" ::: "memory");
;             const unsigned og = xb_add(&bar[XB_TOP], 1u);
;             const unsigned tg = og / nx;
;             if (og + 1u == (tg + 1u) * nx) xb_add(&bar[XB_TOPGEN], 1u);
;             else XB_SPIN(xb_ld(&bar[XB_TOPGEN]) == tg, bar);
;             __builtin_amdgcn_fence(__ATOMIC_ACQUIRE, "agent");
;             xb_add(&bar[XB_XGEN(b.x)], 1u);
;             asm volatile("s_waitcnt vmcnt(0)" ::: "memory");
;         } else {
;             XB_SPIN(xb_ld(&bar[XB_XGEN(b.x)]) == gen, bar);
;             __builtin_amdgcn_fence(__ATOMIC_ACQUIRE, "agent");
;             asm volatile("s_waitcnt vmcnt(0)" ::: "memory");
;         }
;     }
;     __syncthreads();
; }
.LBB0_750:
	v_readlane_b32 s0, v253, 42
	v_readlane_b32 s4, v253, 32
	s_add_i32 s0, s0, 3
	v_readlane_b32 s7, v253, 35
	s_cmp_ge_i32 s0, s7
	v_readlane_b32 s5, v253, 33
	v_readlane_b32 s6, v253, 34
	s_cbranch_scc1 .LBB0_796
	v_readlane_b32 s34, v253, 36
	v_readlane_b32 s35, v253, 37
	s_mov_b32 s1, s76
	s_waitcnt vmcnt(0)
	s_waitcnt vmcnt(0) lgkmcnt(0)
	s_barrier
	s_mov_b64 s[40:41], exec
	v_readlane_b32 s2, v253, 53
	v_readlane_b32 s3, v253, 54
	s_and_b64 s[2:3], s[40:41], s[2:3]
	s_mov_b64 exec, s[2:3]
	s_cbranch_execz .LBB0_795
	v_readlane_b32 s14, v253, 55
	s_nop 3
	s_bitcmp0_b32 s14, 0
	s_cbranch_scc1 .Lgh_old_LBB0_795
	v_readlane_b32 s10, v253, 36
	v_readlane_b32 s11, v253, 37
	v_readlane_b32 s14, v253, 55
	s_nop 3
	s_add_u32 s12, s10, 0xa800
	s_addc_u32 s13, s11, 0
	s_and_b32 s15, s88, 7
	s_lshl_b32 s15, s15, 8
	s_lshr_b32 s14, s14, 1
	s_add_i32 s14, s14, 1
	s_lshl_b32 s14, s14, 5
	v_mov_b32_e32 v2, s15
	v_mov_b32_e32 v5, 1
	global_atomic_add v2, v5, s[12:13]
	s_mov_b32 s18, 0

; __device__ __forceinline__ unsigned xb_ld(unsigned* p)              { return __hip_atomic_load(p, __ATOMIC_RELAXED, __HIP_MEMORY_SCOPE_AGENT); }
; __device__ __forceinline__ unsigned xb_add(unsigned* p, unsigned v) { return __hip_atomic_fetch_add(p, v, __ATOMIC_RELAXED, __HIP_MEMORY_SCOPE_AGENT); }
; #define XB_SPIN(cond, bar) do { unsigned _sp = 0; while (cond) { __builtin_amdgcn_s_sleep(1); \
;     if ((++_sp & 255u) == 0u) { if (xb_ld(&(bar)[XB_TMO])) break; if (_sp > XB_SPIN_CAP) { atomicAdd(&(bar)[XB_TMO], 1u); break; } } } } while (0)
; __device__ __forceinline__ void xcd_barrier(const XcdBarrier& b) {
;     asm volatile("s_waitcnt vmcnt(0)" ::: "memory");
;     __syncthreads();
;     if (threadIdx.x == 0) {
;         unsigned* bar = b.bar;
;         __builtin_amdgcn_s_waitcnt(0);
;         unsigned nloc = b.st[0], nx = b.st[1];
;         if (nloc == 0u) { xcd_barrier_complete(bar, b.x, nloc, nx); b.st[0] = nloc; b.st[1] = nx; }
;         const unsigned old = xb_add(&bar[XB_XSUB(b.x)], 1u);
;         const unsigned gen = old / nloc;
;         if (old + 1u == (gen + 1u) * nloc) {
;             __builtin_amdgcn_fence(__ATOMIC_RELEASE, "agent");
;             asm volatile("s_waitcnt vmcnt(0)" ::: "memory");
;             const unsigned og = xb_add(&bar[XB_TOP], 1u);
;             const unsigned tg = og / nx;
;             if (og + 1u == (tg + 1u) * nx) xb_add(&bar[XB_TOPGEN], 1u);
;             else XB_SPIN(xb_ld(&bar[XB_TOPGEN]) == tg, bar);
;             __builtin_amdgcn_fence(__ATOMIC_ACQUIRE, "agent");
;             xb_add(&bar[XB_XGEN(b.x)], 1u);
;             asm volatile("s_waitcnt vmcnt(0)" ::: "memory");
;         } else {
;             XB_SPIN(xb_ld(&bar[XB_XGEN(b.x)]) == gen, bar);
;             __builtin_amdgcn_fence(__ATOMIC_ACQUIRE, "agent");
;             asm volatile("s_waitcnt vmcnt(0)" ::: "memory");
;         }
;     }
;     __syncthreads();
; }
.Lgh_done_LBB0_795:
	buffer_inv sc1
	s_waitcnt vmcnt(0)
	v_readlane_b32 s10, v253, 36
	v_readlane_b32 s11, v253, 37
	v_readlane_b32 s14, v253, 55
	s_nop 3
	s_mov_b64 exec, 0xff
	s_add_u32 s12, s10, 0xb800
	s_addc_u32 s13, s11, 0
	s_lshr_b32 s14, s14, 0
	s_add_i32 s14, s14, 1
	s_lshl_b32 s14, s14, 5
	v_mbcnt_lo_u32_b32 v4, -1, 0
	v_lshlrev_b32_e32 v4, 8, v4
	s_mov_b32 s18, 0

; __device__ __forceinline__ unsigned xb_add(unsigned* p, unsigned v) { return __hip_atomic_fetch_add(p, v, __ATOMIC_RELAXED, __HIP_MEMORY_SCOPE_AGENT); }
; __device__ __forceinline__ void xcd_barrier(const XcdBarrier& b) {
;     ...
;     if (threadIdx.x == 0) {
;         unsigned* bar = b.bar;
;         __builtin_amdgcn_s_waitcnt(0);
;         unsigned nloc = b.st[0], nx = b.st[1];
;         if (nloc == 0u) { xcd_barrier_complete(bar, b.x, nloc, nx); b.st[0] = nloc; b.st[1] = nx; }
;         const unsigned old = xb_add(&bar[XB_XSUB(b.x)], 1u);
.Lgh_old_LBB0_795:
	v_mov_b32_e32 v2, s77
	s_waitcnt vmcnt(0) expcnt(0) lgkmcnt(0)
	ds_read_b32 v4, v2
	ds_read_b32 v2, v2 offset:4
	s_waitcnt lgkmcnt(1)
	v_cmp_ne_u32_e32 vcc, 0, v4
	s_cbranch_vccnz .LBB0_766
	v_readlane_b32 s2, v253, 38
	v_readlane_b32 s3, v253, 39
	s_load_dwordx2 s[6:7], s[2:3], 0x0
	s_load_dword s5, s[2:3], 0x8
	s_add_u32 s2, s34, 0x1000
	s_addc_u32 s3, s35, 0
	s_add_u32 s4, s34, 0x1100
	s_waitcnt lgkmcnt(0)
	s_mul_i32 s28, s7, s6
	s_mul_i32 s28, s28, s5
	s_addc_u32 s5, s35, 0
	s_add_u32 s6, s34, 0x1200
	s_addc_u32 s7, s35, 0
	s_add_u32 s8, s34, 0x1300
	s_addc_u32 s9, s35, 0
	s_mov_b32 s29, 1
	s_mov_b64 s[10:11], 0
	s_branch .LBB0_756
